# conversion tile loads: scalar row base + 32-bit lane offset instead of a 64-bit vector add per row
# baseline (speedup 1.0000x reference)
; __device__ __forceinline__ void cv_tile_out(const CvTile& cur, LAS float* S, int tid_) {
;     ...
;     const int nbl = cur.N / 256, kb = cur.r / nbl, nb = cur.r - kb * nbl;
.LBB0_461:
	s_lshr_b32 s0, s44, 8
	v_cvt_f32_u32_e32 v0, s0
	s_sub_i32 s23, 0, s0
	s_abs_i32 s22, s18
	s_ashr_i32 s1, s18, 31
	v_rcp_iflag_f32_e32 v0, v0
	v_lshlrev_b32_e32 v2, 2, v132
	v_ashrrev_i32_e32 v3, 31, v2
	s_mov_b32 s45, s90
	v_mul_f32_e32 v0, 0x4f7ffffe, v0
	v_cvt_u32_f32_e32 v0, v0
	s_nop 0
	v_readfirstlane_b32 s27, v0
	s_mul_i32 s23, s23, s27
	s_mul_hi_u32 s23, s27, s23
	s_add_i32 s27, s27, s23
	s_mul_hi_u32 s23, s22, s27
	s_mul_i32 s27, s23, s0
	s_sub_i32 s22, s22, s27
	s_add_i32 s27, s23, 1
	s_sub_i32 s30, s22, s0
	s_cmp_ge_u32 s22, s0
	s_cselect_b32 s23, s27, s23
	s_cselect_b32 s22, s30, s22
	s_add_i32 s27, s23, 1
	s_cmp_ge_u32 s22, s0
	s_cselect_b32 s22, s27, s23
	s_xor_b32 s22, s22, s1
	s_sub_i32 s1, s22, s1
	s_lshl_b32 s56, s1, 7
	s_mul_i32 s0, s1, s0
	s_add_i32 s1, s56, s96
	s_sub_i32 s0, s18, s0
	s_ashr_i32 s18, s1, 31
	s_mul_i32 s18, s18, s44
	s_mul_hi_u32 s22, s1, s44
	s_add_i32 s23, s22, s18
	s_mul_i32 s22, s1, s44
	s_lshl_b64 s[22:23], s[22:23], 2
	s_add_u32 s18, s46, s22
	s_addc_u32 s22, s47, s23
	s_lshl_b32 s84, s0, 8
	s_ashr_i32 s85, s84, 31
	s_lshl_b64 s[0:1], s[84:85], 2
	s_add_u32 s0, s18, s0
	s_addc_u32 s1, s22, s1
	v_lshlrev_b32_e32 v4, 2, v2
	s_lshl_b32 s22, s44, 2
	global_load_dwordx4 v[66:69], v4, s[0:1] nt
	s_add_u32 s0, s0, s22
	s_addc_u32 s1, s1, 0
	global_load_dwordx4 v[70:73], v4, s[0:1] nt
	s_add_u32 s0, s0, s22
	s_addc_u32 s1, s1, 0
	global_load_dwordx4 v[74:77], v4, s[0:1] nt
	s_add_u32 s0, s0, s22
	s_addc_u32 s1, s1, 0
	global_load_dwordx4 v[78:81], v4, s[0:1] nt
	s_add_u32 s0, s0, s22
	s_addc_u32 s1, s1, 0
	global_load_dwordx4 v[82:85], v4, s[0:1] nt
	s_add_u32 s0, s0, s22
	s_addc_u32 s1, s1, 0
	global_load_dwordx4 v[86:89], v4, s[0:1] nt
	s_add_u32 s0, s0, s22
	s_addc_u32 s1, s1, 0
	global_load_dwordx4 v[90:93], v4, s[0:1] nt
	s_add_u32 s0, s0, s22
	s_addc_u32 s1, s1, 0
	global_load_dwordx4 v[94:97], v4, s[0:1] nt
	s_add_u32 s0, s0, s22
	s_addc_u32 s1, s1, 0
	global_load_dwordx4 v[98:101], v4, s[0:1] nt
	s_add_u32 s0, s0, s22
	s_addc_u32 s1, s1, 0
	global_load_dwordx4 v[102:105], v4, s[0:1] nt
	s_add_u32 s0, s0, s22
	s_addc_u32 s1, s1, 0
	global_load_dwordx4 v[106:109], v4, s[0:1] nt
	s_add_u32 s0, s0, s22
	s_addc_u32 s1, s1, 0
	global_load_dwordx4 v[110:113], v4, s[0:1] nt
	s_add_u32 s0, s0, s22
	s_addc_u32 s1, s1, 0
	global_load_dwordx4 v[114:117], v4, s[0:1] nt
	s_add_u32 s0, s0, s22
	s_addc_u32 s1, s1, 0
	global_load_dwordx4 v[118:121], v4, s[0:1] nt
	s_add_u32 s0, s0, s22
	s_addc_u32 s1, s1, 0
	global_load_dwordx4 v[122:125], v4, s[0:1] nt
	s_add_u32 s0, s0, s22
	s_addc_u32 s1, s1, 0
	global_load_dwordx4 v[126:129], v4, s[0:1] nt
	s_and_b64 vcc, exec, s[42:43]
	s_cbranch_vccz .LBB0_473
	s_cmpk_gt_u32 s15, 0xff
	s_mov_b64 s[0:1], -1
	s_cbranch_scc0 .LBB0_471
	s_add_i32 s0, s14, 0xfffffe01
	s_mul_hi_u32 s1, s0, 0x3e0f83e1
	s_lshr_b32 s23, s1, 8
	s_mul_i32 s15, s23, 0xfffffbe0
	s_add_i32 s15, s15, s0
	s_cmpk_gt_i32 s15, 0x15f
	s_mul_hi_u32 s27, s23, 0x2c00000
	s_mul_i32 s28, s23, 0x2c00000
	s_mov_b64 s[0:1], -1
	s_cbranch_scc0 .LBB0_468
	s_mov_b64 s[62:63], -1
	s_cmpk_gt_u32 s15, 0x2bf
	s_cbranch_scc0 .LBB0_466
	s_add_i32 s22, s15, 0xfffffd40
	v_readlane_b32 s0, v254, 49
	v_readlane_b32 s1, v254, 50
	s_add_u32 s44, s0, s28
	s_addc_u32 s45, s1, s27
	s_mul_i32 s1, s23, 0xb00000
	v_readlane_b32 s2, v254, 58
	s_mul_hi_u32 s0, s23, 0xb00000
	s_add_u32 s58, s2, s1
	v_readlane_b32 s1, v254, 59
	s_addc_u32 s59, s1, s0
	s_mov_b64 s[0:1], 0

.LBB0_475:
	s_lshr_b32 s0, s42, 8
	v_cvt_f32_u32_e32 v0, s0
	s_sub_i32 s15, 0, s0
	s_abs_i32 s14, s22
	s_ashr_i32 s1, s22, 31
	v_rcp_iflag_f32_e32 v0, v0
	s_mov_b32 s43, s90
	v_mul_f32_e32 v0, 0x4f7ffffe, v0
	v_cvt_u32_f32_e32 v0, v0
	s_nop 0
	v_readfirstlane_b32 s23, v0
	s_mul_i32 s15, s15, s23
	s_mul_hi_u32 s15, s23, s15
	s_add_i32 s23, s23, s15
	s_mul_hi_u32 s15, s14, s23
	s_mul_i32 s23, s15, s0
	s_sub_i32 s14, s14, s23
	s_add_i32 s23, s15, 1
	s_sub_i32 s27, s14, s0
	s_cmp_ge_u32 s14, s0
	s_cselect_b32 s15, s23, s15
	s_cselect_b32 s14, s27, s14
	s_add_i32 s23, s15, 1
	s_cmp_ge_u32 s14, s0
	s_cselect_b32 s14, s23, s15
	s_xor_b32 s14, s14, s1
	s_sub_i32 s1, s14, s1
	s_lshl_b32 s70, s1, 7
	s_mul_i32 s0, s1, s0
	s_add_i32 s1, s70, s96
	s_ashr_i32 s14, s1, 31
	s_mul_i32 s14, s14, s42
	s_mul_hi_u32 s15, s1, s42
	s_add_i32 s15, s15, s14
	s_mul_i32 s14, s1, s42
	s_sub_i32 s0, s22, s0
	s_lshl_b64 s[14:15], s[14:15], 2
	s_add_u32 s14, s44, s14
	s_addc_u32 s15, s45, s15
	s_lshl_b32 s64, s0, 8
	s_ashr_i32 s65, s64, 31
	s_lshl_b64 s[0:1], s[64:65], 2
	s_add_u32 s0, s14, s0
	s_addc_u32 s1, s15, s1
	v_lshlrev_b32_e32 v0, 2, v2
	s_lshl_b32 s14, s42, 2
	global_load_dwordx4 v[2:5], v0, s[0:1] nt
	s_add_u32 s0, s0, s14
	s_addc_u32 s1, s1, 0
	global_load_dwordx4 v[6:9], v0, s[0:1] nt
	s_add_u32 s0, s0, s14
	s_addc_u32 s1, s1, 0
	global_load_dwordx4 v[10:13], v0, s[0:1] nt
	s_add_u32 s0, s0, s14
	s_addc_u32 s1, s1, 0
	global_load_dwordx4 v[14:17], v0, s[0:1] nt
	s_add_u32 s0, s0, s14
	s_addc_u32 s1, s1, 0
	global_load_dwordx4 v[18:21], v0, s[0:1] nt
	s_add_u32 s0, s0, s14
	s_addc_u32 s1, s1, 0
	global_load_dwordx4 v[22:25], v0, s[0:1] nt
	s_add_u32 s0, s0, s14
	s_addc_u32 s1, s1, 0
	global_load_dwordx4 v[26:29], v0, s[0:1] nt
	s_add_u32 s0, s0, s14
	s_addc_u32 s1, s1, 0
	global_load_dwordx4 v[30:33], v0, s[0:1] nt
	s_add_u32 s0, s0, s14
	s_addc_u32 s1, s1, 0
	global_load_dwordx4 v[34:37], v0, s[0:1] nt
	s_add_u32 s0, s0, s14
	s_addc_u32 s1, s1, 0
	global_load_dwordx4 v[38:41], v0, s[0:1] nt
	s_add_u32 s0, s0, s14
	s_addc_u32 s1, s1, 0
	global_load_dwordx4 v[42:45], v0, s[0:1] nt
	s_add_u32 s0, s0, s14
	s_addc_u32 s1, s1, 0
	global_load_dwordx4 v[46:49], v0, s[0:1] nt
	s_add_u32 s0, s0, s14
	s_addc_u32 s1, s1, 0
	global_load_dwordx4 v[50:53], v0, s[0:1] nt
	s_add_u32 s0, s0, s14
	s_addc_u32 s1, s1, 0
	global_load_dwordx4 v[54:57], v0, s[0:1] nt
	s_add_u32 s0, s0, s14
	s_addc_u32 s1, s1, 0
	global_load_dwordx4 v[58:61], v0, s[0:1] nt
	s_add_u32 s0, s0, s14
	s_addc_u32 s1, s1, 0
	global_load_dwordx4 v[62:65], v0, s[0:1] nt
	s_cmp_eq_u64 s[40:41], 0
	s_cbranch_scc1 .LBB0_477
	s_ashr_i32 s57, s56, 31
	s_lshl_b64 s[0:1], s[56:57], 2
	s_add_u32 s0, s40, s0
	s_addc_u32 s1, s41, s1
	s_lshl_b32 s14, s96, 2
	s_load_dwordx16 s[40:55], s[0:1], s14 offset:0x0
	s_waitcnt lgkmcnt(0)
	s_mov_b32 s0, s43
	s_waitcnt vmcnt(28)
	v_pk_mul_f32 v[80:81], v[80:81], s[0:1] op_sel_hi:[1,0]
	v_pk_mul_f32 v[78:79], v[78:79], s[0:1] op_sel_hi:[1,0]
	s_mov_b32 s0, s45
	s_waitcnt vmcnt(26)
	v_pk_mul_f32 v[88:89], v[88:89], s[0:1] op_sel_hi:[1,0]
	v_pk_mul_f32 v[86:87], v[86:87], s[0:1] op_sel_hi:[1,0]
	s_mov_b32 s0, s47
	s_waitcnt vmcnt(24)
	v_pk_mul_f32 v[96:97], v[96:97], s[0:1] op_sel_hi:[1,0]
	v_pk_mul_f32 v[94:95], v[94:95], s[0:1] op_sel_hi:[1,0]
	s_mov_b32 s0, s49
	s_waitcnt vmcnt(22)
	v_pk_mul_f32 v[104:105], v[104:105], s[0:1] op_sel_hi:[1,0]
	v_pk_mul_f32 v[102:103], v[102:103], s[0:1] op_sel_hi:[1,0]
	s_mov_b32 s0, s51
	s_waitcnt vmcnt(20)
	v_pk_mul_f32 v[112:113], v[112:113], s[0:1] op_sel_hi:[1,0]
	v_pk_mul_f32 v[110:111], v[110:111], s[0:1] op_sel_hi:[1,0]
	s_mov_b32 s0, s53
	s_waitcnt vmcnt(18)
	v_pk_mul_f32 v[120:121], v[120:121], s[0:1] op_sel_hi:[1,0]
	v_pk_mul_f32 v[118:119], v[118:119], s[0:1] op_sel_hi:[1,0]
	s_mov_b32 s0, s55
	v_pk_mul_f32 v[68:69], v[68:69], s[40:41] op_sel_hi:[1,0]
	v_pk_mul_f32 v[66:67], v[66:67], s[40:41] op_sel_hi:[1,0]
	v_pk_mul_f32 v[72:73], v[72:73], s[40:41] op_sel:[0,1]
	v_pk_mul_f32 v[70:71], v[70:71], s[40:41] op_sel:[0,1]
	v_pk_mul_f32 v[76:77], v[76:77], s[42:43] op_sel_hi:[1,0]
	v_pk_mul_f32 v[74:75], v[74:75], s[42:43] op_sel_hi:[1,0]
	v_pk_mul_f32 v[84:85], v[84:85], s[44:45] op_sel_hi:[1,0]
	v_pk_mul_f32 v[82:83], v[82:83], s[44:45] op_sel_hi:[1,0]
	v_pk_mul_f32 v[92:93], v[92:93], s[46:47] op_sel_hi:[1,0]
	v_pk_mul_f32 v[90:91], v[90:91], s[46:47] op_sel_hi:[1,0]
	v_pk_mul_f32 v[100:101], v[100:101], s[48:49] op_sel_hi:[1,0]
	v_pk_mul_f32 v[98:99], v[98:99], s[48:49] op_sel_hi:[1,0]
	v_pk_mul_f32 v[108:109], v[108:109], s[50:51] op_sel_hi:[1,0]
	v_pk_mul_f32 v[106:107], v[106:107], s[50:51] op_sel_hi:[1,0]
	v_pk_mul_f32 v[116:117], v[116:117], s[52:53] op_sel_hi:[1,0]
	v_pk_mul_f32 v[114:115], v[114:115], s[52:53] op_sel_hi:[1,0]
	s_waitcnt vmcnt(17)
	v_pk_mul_f32 v[124:125], v[124:125], s[54:55] op_sel_hi:[1,0]
	v_pk_mul_f32 v[122:123], v[122:123], s[54:55] op_sel_hi:[1,0]
	s_waitcnt vmcnt(16)
	v_pk_mul_f32 v[128:129], v[128:129], s[0:1] op_sel_hi:[1,0]
	v_pk_mul_f32 v[126:127], v[126:127], s[0:1] op_sel_hi:[1,0]
